# attention phases: static s_setprio 1 for waves 0-3 instead of 4-7
# speedup vs baseline: 1.0094x; 1.0094x over previous
.LBB0_544:
	s_cmp_gt_i32 s36, 6
	s_cselect_b64 s[0:1], -1, 0
	s_cmp_lt_i32 s37, 7
	s_cselect_b64 s[2:3], -1, 0
	v_writelane_b32 v255, s80, 2
	s_or_b64 s[0:1], s[0:1], s[2:3]
	v_writelane_b32 v255, s81, 3
	s_and_b64 vcc, exec, s[0:1]
	v_writelane_b32 v255, s82, 4
	s_cbranch_vccnz .LBB0_895
	v_mbcnt_hi_u32_b32 v193, -1, v253
	s_and_b32 s0, s81, 0xffffffc0
	v_add_u32_e32 v184, s0, v193
	s_cmp_gt_u32 s81, 0xff
	s_cbranch_scc1 .Lnoprio_a0
	s_setprio 1

.LBB0_1859:
	s_cmp_gt_i32 s36, 19
	s_cselect_b64 s[0:1], -1, 0
	s_cmp_lt_i32 s37, 20
	s_cselect_b64 s[2:3], -1, 0
	s_or_b64 s[0:1], s[0:1], s[2:3]
	s_and_b64 vcc, exec, s[0:1]
	s_cbranch_vccnz .LBB0_2175
	v_mbcnt_hi_u32_b32 v195, -1, v253
	s_and_b32 s0, s81, 0xffffffc0
	s_cmp_gt_u32 s81, 0xff
	s_cbranch_scc1 .Lnoprio_a1
	s_setprio 1
